# static s_setprio 1 for waves 4-7 set once at kernel entry, all per-phase setprio flips removed
# baseline (speedup 1.0000x reference)
; #define LAS __attribute__((address_space(3)))
; __global__ void __launch_bounds__(NWAVES * 64, 2) mk_fwd(Args args) {
;     extern __shared__ __attribute__((aligned(16))) unsigned char lds[];
;     Frame F;
;     F.lds = (LAS unsigned char*)lds; F.MISC = (volatile LAS unsigned*)(F.lds + MISC_OFF);
;     F.tid = threadIdx.x; F.lane = F.tid & 63; F.wave = __builtin_amdgcn_readfirstlane(F.tid >> 6);
;     F.G = gridDim.x; { const int bx = blockIdx.x; F.vcu = (F.G % 8 == 0) ? (bx % 8) * (F.G / 8) + bx / 8 : bx; }
;     KArgs A = (KArgs)__builtin_amdgcn_kernarg_segment_ptr();
;     unsigned char* ws = A->ws; F.ws = ws; F.ctl = (gu32*)(ws + WS_CTL);
_Z6mk_fwd4Args:
	v_readfirstlane_b32 s5, v0
	s_nop 3
	s_and_b32 s5, s5, 0x3ff
	s_lshr_b32 s5, s5, 6
	s_cmp_ge_u32 s5, 4
	s_cbranch_scc0 .Lprio_done
	s_setprio 1
.Lprio_done:
	s_load_dword s33, s[0:1], 0x160
	s_mov_b64 s[66:67], s[0:1]
	s_add_u32 s0, s66, 0x160
	s_addc_u32 s1, s67, 0
	s_mov_b32 s4, 0
	v_writelane_b32 v253, s0, 0
	s_waitcnt lgkmcnt(0)
	s_and_b32 s3, s33, 7
	s_cmp_eq_u32 s3, 0
	v_writelane_b32 v253, s1, 1
	s_cselect_b64 s[0:1], -1, 0
	s_cmp_lg_u32 s3, 0
	v_writelane_b32 v253, s2, 2
	s_cbranch_scc1 .LBB0_2
	s_ashr_i32 s5, s2, 31
	s_lshr_b32 s5, s5, 29
	s_add_i32 s5, s2, s5
	s_and_b32 s6, s5, -8
	s_ashr_i32 s3, s33, 3
	s_sub_i32 s6, s2, s6
	s_mul_i32 s3, s3, s6
	s_ashr_i32 s5, s5, 3
	s_add_i32 s3, s3, s5
	v_writelane_b32 v253, s3, 2
